# stick-breaking loop: s_setprio brackets around its four MFMA bursts (on top of the DA brackets)
# baseline (speedup 1.0000x reference)
; #define LAS __attribute__((address_space(3)))
; __device__ __forceinline__ int crow(int r, int hi) { return (r & 3) + 8 * (r >> 2) + 4 * hi; }
; template <bool MASK> __device__ __forceinline__ void sb_block(f32x16& p, float& running, int kofs, int lo, int lim, int hi) {
;     constexpr float C1 = 0.08838834764831845f * 1.4426950408889634f;
;     float L[16];
; #pragma unroll
;     for (int r = 0; r < 16; ++r) { const float z2 = p[r] * C1, t = __builtin_amdgcn_exp2f(-fabsf(z2)); const float sp = fmaxf(z2, 0.f) + __builtin_amdgcn_logf(1.0f + t);
;         const int kk = kofs + crow(r, hi); const bool valid = !MASK || (kk >= lo && kk < lim);
;         L[r] = valid ? -sp : 0.f; p[r] = valid ? z2 : -1.0e30f; }
; __device__ __forceinline__ void sb_unit(LAS unsigned char* lds, const bf16* __restrict__ Q, const bf16* __restrict__ Kp, const bf16* __restrict__ Vp, const float* __restrict__ gsb,
;                                         bf16* __restrict__ mixed, int b, int h, int qt, int tid, int wave, int lane) {
;     ...
;         if (!done && j <= jw) {
;             const bool need_mask = (j == jw) || (j == 0);
;             const int lim = Prow - 64 * j, lo = (j == 0) ? KVPAD : 0;
;             float running = carry;
;             const LAS unsigned char* Ks = K_lds + buf * SHM_T;
;             {   f32x16 p;
; #pragma unroll
;                 for (int r = 0; r < 16; ++r) p[r] = 0.f;
; #pragma unroll
;                 for (int d0 = 0; d0 < 8; ++d0) { const int ko = kb[d0 & 3] + (d0 >> 2) * 128;
;                     const bf16x8 b1 = *(const LAS bf16x8*)(Ks + ko + 8192), qv = *(const LAS bf16x8*)(Qs + ko); p = __builtin_amdgcn_mfma_f32_32x32x16_bf16(b1, qv, p, 0, 0, 0); }
;                 if (need_mask) sb_block<true>(p, running, 32, lo, lim, hi); else sb_block<false>(p, running, 32, lo, lim, hi);
.LBB0_613:
	s_xor_b64 s[6:7], s[6:7], -1
	s_andn2_b64 vcc, exec, s[6:7]
	s_mov_b64 s[6:7], -1
	s_cbranch_vccnz .LBB0_624
	s_cmp_gt_i32 s25, s66
	s_mov_b64 s[6:7], 0
	s_cbranch_scc1 .LBB0_624
	s_add_i32 s6, s39, s70
	s_cmp_lg_u32 s6, 0
	s_cselect_b64 s[8:9], -1, 0
	s_lshl_b32 s73, s72, 14
	s_add_i32 s6, s73, 0
	v_add_u32_e32 v112, s6, v115
	ds_read_b128 v[68:71], v112 offset:40960
	v_add_u32_e32 v190, s60, v115
	ds_read_b128 v[72:75], v190
	ds_read_b128 v[84:87], v190 offset:128
	v_add_u32_e32 v191, s6, v116
	ds_read_b128 v[88:91], v112 offset:41088
	ds_read_b128 v[92:95], v191 offset:40960
	v_add_u32_e32 v192, s60, v116
	ds_read_b128 v[96:99], v192
	ds_read_b128 v[198:201], v192 offset:128
	s_waitcnt lgkmcnt(5)
	s_setprio 1
	v_mfma_f32_32x32x16_bf16 v[68:83], v[68:71], v[72:75], 0
	v_add_u32_e32 v193, s6, v117
	ds_read_b128 v[202:205], v191 offset:41088
	v_add_u32_e32 v195, s60, v117
	v_add_u32_e32 v196, s6, v118
	v_add_u32_e32 v197, s60, v118
	s_xor_b64 s[14:15], s[26:27], -1
	s_and_b64 s[22:23], s[8:9], s[14:15]
	s_waitcnt lgkmcnt(2)
	v_mfma_f32_32x32x16_bf16 v[68:83], v[92:95], v[96:99], v[68:83]
	ds_read_b128 v[92:95], v193 offset:40960
	ds_read_b128 v[96:99], v195
	ds_read_b128 v[206:209], v195 offset:128
	ds_read_b128 v[210:213], v193 offset:41088
	s_and_b64 s[8:9], exec, s[26:27]
	s_mov_b64 s[6:7], -1
	s_cselect_b32 s26, 48, 0
	s_and_b64 vcc, exec, s[22:23]
	s_waitcnt lgkmcnt(2)
	v_mfma_f32_32x32x16_bf16 v[68:83], v[92:95], v[96:99], v[68:83]
	ds_read_b128 v[92:95], v196 offset:40960
	ds_read_b128 v[96:99], v197
	ds_read_b128 v[214:217], v197 offset:128
	ds_read_b128 v[218:221], v196 offset:41088
	s_waitcnt lgkmcnt(2)
	v_mfma_f32_32x32x16_bf16 v[68:83], v[92:95], v[96:99], v[68:83]
	v_mfma_f32_32x32x16_bf16 v[68:83], v[88:91], v[84:87], v[68:83]
	v_mfma_f32_32x32x16_bf16 v[68:83], v[202:205], v[198:201], v[68:83]
	v_mfma_f32_32x32x16_bf16 v[68:83], v[210:213], v[206:209], v[68:83]
	s_waitcnt lgkmcnt(0)
	v_mfma_f32_32x32x16_bf16 v[68:83], v[218:221], v[214:217], v[68:83]
	s_setprio 0
	s_nop 11
	v_mul_f32_e32 v212, 0x3e0293ee, v68
	v_exp_f32_e64 v3, -|v212|
	v_max_f32_e32 v110, 0, v212
	v_mul_f32_e32 v211, 0x3e0293ee, v69
	v_mul_f32_e32 v210, 0x3e0293ee, v70
	v_add_f32_e32 v3, 1.0, v3
	v_log_f32_e32 v68, v3
	v_mul_f32_e32 v209, 0x3e0293ee, v71
	v_mul_f32_e32 v208, 0x3e0293ee, v72
	v_mul_f32_e32 v207, 0x3e0293ee, v73
	v_mul_f32_e32 v206, 0x3e0293ee, v74
	v_mul_f32_e32 v205, 0x3e0293ee, v75
	v_mul_f32_e32 v204, 0x3e0293ee, v76
	v_mul_f32_e32 v203, 0x3e0293ee, v77
	v_mul_f32_e32 v202, 0x3e0293ee, v78
	v_mul_f32_e32 v201, 0x3e0293ee, v79
	v_mul_f32_e32 v200, 0x3e0293ee, v80
	v_mul_f32_e32 v199, 0x3e0293ee, v81
	v_mul_f32_e32 v198, 0x3e0293ee, v82
	v_mul_f32_e32 v3, 0x3e0293ee, v83
	v_add_f32_e32 v68, v110, v68
	s_cbranch_vccz .LBB0_617
; __device__ __forceinline__ int crow(int r, int hi) { return (r & 3) + 8 * (r >> 2) + 4 * hi; }
; template <bool MASK> __device__ __forceinline__ void sb_block(f32x16& p, float& running, int kofs, int lo, int lim, int hi) {
;     constexpr float C1 = 0.08838834764831845f * 1.4426950408889634f;
;     float L[16];
; #pragma unroll
;     for (int r = 0; r < 16; ++r) { const float z2 = p[r] * C1, t = __builtin_amdgcn_exp2f(-fabsf(z2)); const float sp = fmaxf(z2, 0.f) + __builtin_amdgcn_logf(1.0f + t);
;         const int kk = kofs + crow(r, hi); const bool valid = !MASK || (kk >= lo && kk < lim);
;         L[r] = valid ? -sp : 0.f; p[r] = valid ? z2 : -1.0e30f; }
;     float G[4], PG[4];
; #pragma unroll
;     for (int g = 0; g < 4; ++g) { G[g] = (L[4 * g] + L[4 * g + 1]) + (L[4 * g + 2] + L[4 * g + 3]); PG[g] = __shfl_xor(G[g], 32); }
; #pragma unroll
;     for (int g = 3; g >= 0; --g) { const float off = running + (hi == 0 ? PG[g] : 0.f);
;         const float c3 = L[4 * g + 3] + off, c2 = L[4 * g + 2] + c3, c1 = L[4 * g + 1] + c2, c0 = L[4 * g] + c1;
;         p[4 * g + 3] = __builtin_amdgcn_exp2f(p[4 * g + 3] + c3); p[4 * g + 2] = __builtin_amdgcn_exp2f(p[4 * g + 2] + c2);
;         p[4 * g + 1] = __builtin_amdgcn_exp2f(p[4 * g + 1] + c1); p[4 * g] = __builtin_amdgcn_exp2f(p[4 * g] + c0);
;         running += G[g] + PG[g]; }
; }
	v_exp_f32_e64 v84, -|v211|
	v_exp_f32_e64 v87, -|v209|
	v_exp_f32_e64 v86, -|v210|
	v_max_f32_e32 v85, 0, v211
	v_add_f32_e32 v84, 1.0, v84
	v_log_f32_e32 v88, v84
	v_add_f32_e32 v87, 1.0, v87
	v_log_f32_e32 v87, v87
	v_max_f32_e32 v92, 0, v207
	v_add_f32_e32 v213, v85, v88
	v_add_f32_e32 v85, 1.0, v86
	v_log_f32_e32 v86, v85
	v_max_f32_e32 v85, 0, v209
	v_add_f32_e32 v226, v85, v87
	v_exp_f32_e64 v85, -|v208|
	v_exp_f32_e64 v87, -|v207|
	v_max_f32_e32 v88, 0, v208
	v_max_f32_e32 v89, 0, v206
	v_add_f32_e32 v85, 1.0, v85
	v_log_f32_e32 v90, v85
	v_add_f32_e32 v85, 1.0, v87
	v_exp_f32_e64 v87, -|v206|
	v_log_f32_e32 v94, v85
	v_exp_f32_e64 v85, -|v205|
	v_max_f32_e32 v93, 0, v205
	v_add_f32_e32 v87, 1.0, v87
	v_log_f32_e32 v91, v87
	v_add_f32_e32 v85, 1.0, v85
	v_exp_f32_e64 v87, -|v204|
	v_log_f32_e32 v95, v85
	v_exp_f32_e64 v85, -|v203|
	v_pk_add_f32 v[88:89], v[88:89], v[90:91]
	v_add_f32_e32 v87, 1.0, v87
	v_log_f32_e32 v98, v87
	v_add_f32_e32 v85, 1.0, v85
	v_exp_f32_e64 v87, -|v202|
	v_log_f32_e32 v216, v85
	v_exp_f32_e64 v85, -|v201|
	v_pk_add_f32 v[90:91], v[92:93], v[94:95]
	v_add_f32_e32 v87, 1.0, v87
	v_log_f32_e32 v99, v87
	v_add_f32_e32 v85, 1.0, v85
	v_exp_f32_e64 v87, -|v200|
	v_log_f32_e32 v217, v85
	v_exp_f32_e64 v85, -|v199|
	v_max_f32_e32 v96, 0, v204
	v_add_f32_e32 v87, 1.0, v87
	v_log_f32_e32 v220, v87
	v_add_f32_e32 v85, 1.0, v85
	v_exp_f32_e64 v87, -|v198|
	v_log_f32_e32 v224, v85
	v_exp_f32_e64 v85, -|v3|
	v_max_f32_e32 v97, 0, v202
	v_add_f32_e32 v87, 1.0, v87
	v_log_f32_e32 v221, v87
	v_add_f32_e32 v85, 1.0, v85
	v_log_f32_e32 v225, v85
	v_and_b32_e32 v87, 64, v160
	v_xor_b32_e32 v85, 32, v160
	v_add_u32_e32 v87, 64, v87
	v_cmp_lt_i32_e32 vcc, v85, v87
	v_max_f32_e32 v218, 0, v200
	v_max_f32_e32 v222, 0, v199
	v_max_f32_e32 v219, 0, v198
	v_max_f32_e32 v223, 0, v3
	v_cndmask_b32_e32 v85, v160, v85, vcc
	v_pk_add_f32 v[92:93], v[90:91], v[88:89] neg_lo:[1,1] neg_hi:[1,1]
	v_lshlrev_b32_e32 v227, 2, v85
	v_add_f32_e32 v85, v92, v93
	v_pk_add_f32 v[92:93], v[96:97], v[98:99]
	v_pk_add_f32 v[94:95], v[218:219], v[220:221]
	v_pk_add_f32 v[96:97], v[222:223], v[224:225]
	v_max_f32_e32 v214, 0, v203
	v_pk_add_f32 v[98:99], v[96:97], v[94:95] neg_lo:[1,1] neg_hi:[1,1]
	v_max_f32_e32 v215, 0, v201
	v_pk_add_f32 v[218:219], v[98:99], v[98:99] op_sel:[0,1] op_sel_hi:[1,0]
	ds_bpermute_b32 v87, v227, v218
	v_pk_add_f32 v[214:215], v[214:215], v[216:217]
	ds_bpermute_b32 v228, v227, v85
	v_pk_add_f32 v[98:99], v[214:215], v[92:93] neg_lo:[1,1] neg_hi:[1,1]
	v_max_f32_e32 v84, 0, v210
	v_pk_add_f32 v[216:217], v[98:99], v[98:99] op_sel:[0,1] op_sel_hi:[1,0]
	s_waitcnt lgkmcnt(1)
	v_cndmask_b32_e64 v98, 0, v87, s[0:1]
	v_add_f32_e32 v98, v111, v98
	ds_bpermute_b32 v113, v227, v216
	v_sub_f32_e32 v97, v98, v97
	v_sub_f32_e32 v95, v97, v95
	v_sub_f32_e32 v96, v95, v96
	v_sub_f32_e32 v94, v96, v94
	v_fmac_f32_e32 v96, 0x3e0293ee, v81
	s_waitcnt lgkmcnt(1)
	v_add_f32_e32 v81, v85, v228
	v_mov_b32_e32 v85, v218
	v_xor_b32_e32 v110, 0x80000000, v226
	v_fmac_f32_e32 v97, 0x3e0293ee, v83
	v_fmac_f32_e32 v95, 0x3e0293ee, v82
	v_pk_add_f32 v[82:83], v[84:85], v[86:87]
	s_waitcnt lgkmcnt(0)
	v_cndmask_b32_e64 v219, 0, v113, s[0:1]
	v_pk_add_f32 v[86:87], v[110:111], v[82:83]
	v_pk_add_f32 v[84:85], v[110:111], v[82:83] neg_lo:[0,1] neg_hi:[0,1]
	v_add_f32_e32 v83, v219, v87
	v_sub_f32_e32 v83, v83, v215
	v_fmac_f32_e32 v94, 0x3e0293ee, v80
	v_pk_add_f32 v[216:217], v[216:217], v[112:113] op_sel_hi:[0,1]
	v_sub_f32_e32 v86, v83, v93
	v_exp_f32_e32 v99, v97
	v_exp_f32_e32 v98, v95
	v_exp_f32_e32 v97, v96
	v_exp_f32_e32 v96, v94
	v_mov_b32_e32 v85, v87
	v_sub_f32_e64 v94, -v213, v68
	v_mov_b32_e32 v95, v217
	v_sub_f32_e32 v87, v86, v214
	v_cndmask_b32_e64 v220, 0, v228, s[0:1]
	v_pk_add_f32 v[84:85], v[94:95], v[84:85]
	v_sub_f32_e32 v92, v87, v92
	ds_bpermute_b32 v80, v227, v84
	v_fmac_f32_e32 v92, 0x3e0293ee, v76
	v_add_f32_e32 v76, v220, v85
	v_sub_f32_e32 v76, v76, v91
	v_fmac_f32_e32 v87, 0x3e0293ee, v77
	v_sub_f32_e32 v77, v76, v89
	v_fmac_f32_e32 v86, 0x3e0293ee, v78
	v_sub_f32_e32 v78, v77, v90
	v_fmac_f32_e32 v83, 0x3e0293ee, v79
	v_sub_f32_e32 v79, v78, v88
	v_fmac_f32_e32 v77, 0x3e0293ee, v74
	v_fmac_f32_e32 v78, 0x3e0293ee, v73
	v_fmac_f32_e32 v79, 0x3e0293ee, v72
	s_waitcnt lgkmcnt(0)
	v_cndmask_b32_e64 v74, 0, v80, s[0:1]
	v_pk_add_f32 v[72:73], v[84:85], v[80:81]
	v_fmac_f32_e32 v76, 0x3e0293ee, v75
	v_add_f32_e32 v74, v74, v73
	v_sub_f32_e32 v74, v74, v226
	v_sub_f32_e32 v75, v74, v82
	v_exp_f32_e32 v91, v76
	v_sub_f32_e32 v76, v75, v213
	v_exp_f32_e32 v90, v77
	v_sub_f32_e32 v77, v76, v68
	v_fmac_f32_e32 v74, 0x3e0293ee, v71
	v_fmac_f32_e32 v75, 0x3e0293ee, v70
	v_fmac_f32_e32 v76, 0x3e0293ee, v69
	v_add_f32_e32 v69, v212, v77
	v_exp_f32_e32 v95, v83
	v_exp_f32_e32 v94, v86
	v_exp_f32_e32 v93, v87
	v_exp_f32_e32 v92, v92
	v_exp_f32_e32 v89, v78
	v_exp_f32_e32 v88, v79
	v_exp_f32_e32 v87, v74
	v_exp_f32_e32 v86, v75
	v_exp_f32_e32 v85, v76
	v_exp_f32_e32 v84, v69
	v_add_f32_e32 v113, v72, v73
	s_mov_b64 s[6:7], 0

; #define LAS __attribute__((address_space(3)))
; #define SBAR() __builtin_amdgcn_sched_barrier(0)
; #define ATT_RDK(X, KS) do { X##0 = tr_read<v_rd_off(0, KS, 0)>(vb); X##1 = tr_read<v_rd_off(0, KS, 1)>(vb); X##2 = tr_read<v_rd_off(1, KS, 0)>(vb); X##3 = tr_read<v_rd_off(1, KS, 1)>(vb); \
;     X##4 = tr_read<v_rd_off(2, KS, 0)>(vb); X##5 = tr_read<v_rd_off(2, KS, 1)>(vb); X##6 = tr_read<v_rd_off(3, KS, 0)>(vb); X##7 = tr_read<v_rd_off(3, KS, 1)>(vb); } while (0)
; #define ATT_MMAK(PA, X) do { o[0] = __builtin_amdgcn_mfma_f32_32x32x16_bf16(PA, ATT_PKV(X##0, X##1), o[0], 0, 0, 0); o[1] = __builtin_amdgcn_mfma_f32_32x32x16_bf16(PA, ATT_PKV(X##2, X##3), o[1], 0, 0, 0); \
;     o[2] = __builtin_amdgcn_mfma_f32_32x32x16_bf16(PA, ATT_PKV(X##4, X##5), o[2], 0, 0, 0); o[3] = __builtin_amdgcn_mfma_f32_32x32x16_bf16(PA, ATT_PKV(X##6, X##7), o[3], 0, 0, 0); } while (0)
; template <int BLK> __device__ __forceinline__ void pv_half(f32x16* o, int vb, bf16x8 paA, bf16x8 paB) {
;     s16x4 a0, a1, a2, a3, a4, a5, a6, a7, b0, b1, b2, b3, b4, b5, b6, b7;
;     SBAR(); ATT_RDK(a, 2 * BLK); ATT_RDK(b, 2 * BLK + 1);
;     asm volatile("s_waitcnt lgkmcnt(8)" ::: "memory"); SBAR(); ATT_MMAK(paA, a);
;     asm volatile("s_waitcnt lgkmcnt(0)" ::: "memory"); SBAR(); ATT_MMAK(paB, b);
; }
; __device__ __forceinline__ void sb_unit(LAS unsigned char* lds, const bf16* __restrict__ Q, const bf16* __restrict__ Kp, const bf16* __restrict__ Vp, const float* __restrict__ gsb,
;                                         bf16* __restrict__ mixed, int b, int h, int qt, int tid, int wave, int lane) {
;     ...
;                 bf16x8 paA, paB; ATT_PK4(p, 0, paA); ATT_PK4(p, 8, paB);
;                 pv_half<1>(o, vb0 + buf * SHM_T, paA, paB); }
;             SBAR();
;             {   f32x16 p;
; #pragma unroll
;                 for (int r = 0; r < 16; ++r) p[r] = 0.f;
; #pragma unroll
;                 for (int d0 = 0; d0 < 8; ++d0) { const int ko = kb[d0 & 3] + (d0 >> 2) * 128;
;                     const bf16x8 b0 = *(const LAS bf16x8*)(Ks + ko), qv = *(const LAS bf16x8*)(Qs + ko); p = __builtin_amdgcn_mfma_f32_32x32x16_bf16(b0, qv, p, 0, 0, 0); }
;                 if (need_mask) sb_block<true>(p, running, 0, lo, lim, hi); else sb_block<false>(p, running, 0, lo, lim, hi);
.LBB0_619:
	v_cvt_pk_bf16_f32 v68, v84, v85
	v_cvt_pk_bf16_f32 v69, v86, v87
	v_cvt_pk_bf16_f32 v70, v88, v89
	v_cvt_pk_bf16_f32 v71, v90, v91
	v_cvt_pk_bf16_f32 v72, v92, v93
	v_cvt_pk_bf16_f32 v73, v94, v95
	v_cvt_pk_bf16_f32 v74, v96, v97
	v_cvt_pk_bf16_f32 v75, v98, v99
	v_permlane32_swap_b32_e32 v68, v70
	v_permlane32_swap_b32_e32 v69, v71
	v_permlane32_swap_b32_e32 v72, v74
	v_permlane32_swap_b32_e32 v73, v75
	v_add_u32_e32 v3, s73, v148
	ds_read_b64_tr_b16 v[76:77], v3 offset:0x2000
	ds_read_b64_tr_b16 v[78:79], v3 offset:0x2800
	ds_read_b64_tr_b16 v[80:81], v3 offset:0x2200
	ds_read_b64_tr_b16 v[82:83], v3 offset:0x2a00
	ds_read_b64_tr_b16 v[84:85], v3 offset:0x2400
	ds_read_b64_tr_b16 v[86:87], v3 offset:0x2c00
	ds_read_b64_tr_b16 v[88:89], v3 offset:0x2600
	ds_read_b64_tr_b16 v[90:91], v3 offset:0x2e00
	ds_read_b64_tr_b16 v[92:93], v3 offset:0x3000
	ds_read_b64_tr_b16 v[94:95], v3 offset:0x3800
	ds_read_b64_tr_b16 v[96:97], v3 offset:0x3200
	ds_read_b64_tr_b16 v[98:99], v3 offset:0x3a00
	ds_read_b64_tr_b16 v[198:199], v3 offset:0x3400
	ds_read_b64_tr_b16 v[200:201], v3 offset:0x3c00
	ds_read_b64_tr_b16 v[202:203], v3 offset:0x3600
	ds_read_b64_tr_b16 v[204:205], v3 offset:0x3e00
	s_waitcnt lgkmcnt(8)
	s_nop 0
	s_setprio 1
	v_mfma_f32_32x32x16_bf16 v[52:67], v[68:71], v[76:79], v[52:67]
	s_waitcnt lgkmcnt(0)
	v_mfma_f32_32x32x16_bf16 v[20:35], v[68:71], v[80:83], v[20:35]
	v_mfma_f32_32x32x16_bf16 v[36:51], v[68:71], v[84:87], v[36:51]
	v_mfma_f32_32x32x16_bf16 v[4:19], v[68:71], v[88:91], v[4:19]
	v_mfma_f32_32x32x16_bf16 v[52:67], v[72:75], v[92:95], v[52:67]
	v_mfma_f32_32x32x16_bf16 v[20:35], v[72:75], v[96:99], v[20:35]
	v_mfma_f32_32x32x16_bf16 v[36:51], v[72:75], v[198:201], v[36:51]
	v_mfma_f32_32x32x16_bf16 v[4:19], v[72:75], v[202:205], v[4:19]
	s_setprio 0
	ds_read_b128 v[68:71], v112 offset:32768
	ds_read_b128 v[72:75], v190
	ds_read_b128 v[84:87], v112 offset:32896
	ds_read_b128 v[88:91], v190 offset:128
	ds_read_b128 v[92:95], v191 offset:32768
	ds_read_b128 v[96:99], v192
	ds_read_b128 v[198:201], v191 offset:32896
	ds_read_b128 v[202:205], v192 offset:128
	s_mov_b64 s[6:7], -1
	s_waitcnt lgkmcnt(6)
	s_setprio 1
	v_mfma_f32_32x32x16_bf16 v[68:83], v[68:71], v[72:75], 0
	s_and_b64 vcc, exec, s[22:23]
	s_waitcnt lgkmcnt(2)
	v_mfma_f32_32x32x16_bf16 v[68:83], v[92:95], v[96:99], v[68:83]
	ds_read_b128 v[92:95], v193 offset:32768
	ds_read_b128 v[96:99], v195
	ds_read_b128 v[190:193], v193 offset:32896
	ds_read_b128 v[206:209], v195 offset:128
	s_waitcnt lgkmcnt(2)
	v_mfma_f32_32x32x16_bf16 v[68:83], v[92:95], v[96:99], v[68:83]
	ds_read_b128 v[92:95], v196 offset:32768
	ds_read_b128 v[96:99], v197
	ds_read_b128 v[210:213], v196 offset:32896
	ds_read_b128 v[214:217], v197 offset:128
	s_waitcnt lgkmcnt(2)
	v_mfma_f32_32x32x16_bf16 v[68:83], v[92:95], v[96:99], v[68:83]
	v_mfma_f32_32x32x16_bf16 v[68:83], v[84:87], v[88:91], v[68:83]
	v_mfma_f32_32x32x16_bf16 v[68:83], v[198:201], v[202:205], v[68:83]
	v_mfma_f32_32x32x16_bf16 v[68:83], v[190:193], v[206:209], v[68:83]
	s_waitcnt lgkmcnt(0)
	v_mfma_f32_32x32x16_bf16 v[68:83], v[210:213], v[214:217], v[68:83]
	s_setprio 0
	s_nop 11
	v_mul_f32_e32 v205, 0x3e0293ee, v68
	v_exp_f32_e64 v68, -|v205|
	v_max_f32_e32 v112, 0, v205
	v_mul_f32_e32 v204, 0x3e0293ee, v69
	v_mul_f32_e32 v203, 0x3e0293ee, v70
	v_add_f32_e32 v68, 1.0, v68
	v_log_f32_e32 v68, v68
	v_mul_f32_e32 v202, 0x3e0293ee, v71
	v_mul_f32_e32 v201, 0x3e0293ee, v72
	v_mul_f32_e32 v200, 0x3e0293ee, v73
	v_mul_f32_e32 v199, 0x3e0293ee, v74
	v_mul_f32_e32 v198, 0x3e0293ee, v75
	v_mul_f32_e32 v197, 0x3e0293ee, v76
	v_mul_f32_e32 v196, 0x3e0293ee, v77
	v_mul_f32_e32 v195, 0x3e0293ee, v78
	v_mul_f32_e32 v193, 0x3e0293ee, v79
	v_mul_f32_e32 v192, 0x3e0293ee, v80
	v_mul_f32_e32 v191, 0x3e0293ee, v81
	v_mul_f32_e32 v190, 0x3e0293ee, v82
	v_mul_f32_e32 v110, 0x3e0293ee, v83
	v_add_f32_e32 v68, v112, v68
	s_cbranch_vccz .LBB0_621
; __device__ __forceinline__ int crow(int r, int hi) { return (r & 3) + 8 * (r >> 2) + 4 * hi; }
; template <bool MASK> __device__ __forceinline__ void sb_block(f32x16& p, float& running, int kofs, int lo, int lim, int hi) {
;     constexpr float C1 = 0.08838834764831845f * 1.4426950408889634f;
;     float L[16];
; #pragma unroll
;     for (int r = 0; r < 16; ++r) { const float z2 = p[r] * C1, t = __builtin_amdgcn_exp2f(-fabsf(z2)); const float sp = fmaxf(z2, 0.f) + __builtin_amdgcn_logf(1.0f + t);
;         const int kk = kofs + crow(r, hi); const bool valid = !MASK || (kk >= lo && kk < lim);
;         L[r] = valid ? -sp : 0.f; p[r] = valid ? z2 : -1.0e30f; }
;     float G[4], PG[4];
; #pragma unroll
;     for (int g = 0; g < 4; ++g) { G[g] = (L[4 * g] + L[4 * g + 1]) + (L[4 * g + 2] + L[4 * g + 3]); PG[g] = __shfl_xor(G[g], 32); }
; #pragma unroll
;     for (int g = 3; g >= 0; --g) { const float off = running + (hi == 0 ? PG[g] : 0.f);
;         const float c3 = L[4 * g + 3] + off, c2 = L[4 * g + 2] + c3, c1 = L[4 * g + 1] + c2, c0 = L[4 * g] + c1;
;         p[4 * g + 3] = __builtin_amdgcn_exp2f(p[4 * g + 3] + c3); p[4 * g + 2] = __builtin_amdgcn_exp2f(p[4 * g + 2] + c2);
;         p[4 * g + 1] = __builtin_amdgcn_exp2f(p[4 * g + 1] + c1); p[4 * g] = __builtin_amdgcn_exp2f(p[4 * g] + c0);
;         running += G[g] + PG[g]; }
; }
	v_exp_f32_e64 v84, -|v204|
	v_exp_f32_e64 v87, -|v202|
	v_exp_f32_e64 v86, -|v203|
	v_max_f32_e32 v85, 0, v204
	v_add_f32_e32 v84, 1.0, v84
	v_log_f32_e32 v88, v84
	v_add_f32_e32 v87, 1.0, v87
	v_log_f32_e32 v87, v87
	v_max_f32_e32 v92, 0, v200
	v_add_f32_e32 v218, v85, v88
	v_add_f32_e32 v85, 1.0, v86
	v_log_f32_e32 v86, v85
	v_max_f32_e32 v85, 0, v202
	v_add_f32_e32 v219, v85, v87
	v_exp_f32_e64 v85, -|v201|
	v_exp_f32_e64 v87, -|v200|
	v_max_f32_e32 v88, 0, v201
	v_max_f32_e32 v89, 0, v199
	v_add_f32_e32 v85, 1.0, v85
	v_log_f32_e32 v90, v85
	v_add_f32_e32 v85, 1.0, v87
	v_exp_f32_e64 v87, -|v199|
	v_log_f32_e32 v94, v85
	v_exp_f32_e64 v85, -|v198|
	v_max_f32_e32 v93, 0, v198
	v_add_f32_e32 v87, 1.0, v87
	v_log_f32_e32 v91, v87
	v_add_f32_e32 v85, 1.0, v85
	v_exp_f32_e64 v87, -|v197|
	v_log_f32_e32 v95, v85
	v_exp_f32_e64 v85, -|v196|
	v_pk_add_f32 v[88:89], v[88:89], v[90:91]
	v_add_f32_e32 v87, 1.0, v87
	v_log_f32_e32 v98, v87
	v_add_f32_e32 v85, 1.0, v85
	v_exp_f32_e64 v87, -|v195|
	v_log_f32_e32 v208, v85
	v_exp_f32_e64 v85, -|v193|
	v_pk_add_f32 v[90:91], v[92:93], v[94:95]
	v_add_f32_e32 v87, 1.0, v87
	v_log_f32_e32 v99, v87
	v_add_f32_e32 v85, 1.0, v85
	v_exp_f32_e64 v87, -|v192|
	v_log_f32_e32 v209, v85
	v_exp_f32_e64 v85, -|v191|
	v_max_f32_e32 v96, 0, v197
	v_add_f32_e32 v87, 1.0, v87
	v_log_f32_e32 v212, v87
	v_add_f32_e32 v85, 1.0, v85
	v_exp_f32_e64 v87, -|v190|
	v_log_f32_e32 v216, v85
	v_exp_f32_e64 v85, -|v110|
	v_max_f32_e32 v97, 0, v195
	v_add_f32_e32 v87, 1.0, v87
	v_log_f32_e32 v213, v87
	v_add_f32_e32 v85, 1.0, v85
	v_log_f32_e32 v217, v85
	v_and_b32_e32 v87, 64, v160
	v_xor_b32_e32 v85, 32, v160
	v_add_u32_e32 v87, 64, v87
	v_cmp_lt_i32_e32 vcc, v85, v87
	v_max_f32_e32 v210, 0, v192
	v_max_f32_e32 v214, 0, v191
	v_max_f32_e32 v211, 0, v190
	v_max_f32_e32 v215, 0, v110
	v_cndmask_b32_e32 v85, v160, v85, vcc
	v_pk_add_f32 v[92:93], v[90:91], v[88:89] neg_lo:[1,1] neg_hi:[1,1]
	v_lshlrev_b32_e32 v220, 2, v85
	v_add_f32_e32 v85, v92, v93
	v_pk_add_f32 v[92:93], v[96:97], v[98:99]
	v_pk_add_f32 v[94:95], v[210:211], v[212:213]
	v_pk_add_f32 v[96:97], v[214:215], v[216:217]
	v_max_f32_e32 v206, 0, v196
	v_pk_add_f32 v[98:99], v[96:97], v[94:95] neg_lo:[1,1] neg_hi:[1,1]
	v_max_f32_e32 v207, 0, v193
	v_pk_add_f32 v[210:211], v[98:99], v[98:99] op_sel:[0,1] op_sel_hi:[1,0]
	ds_bpermute_b32 v87, v220, v210
	v_pk_add_f32 v[206:207], v[206:207], v[208:209]
	ds_bpermute_b32 v221, v220, v85
	v_pk_add_f32 v[98:99], v[206:207], v[92:93] neg_lo:[1,1] neg_hi:[1,1]
	v_max_f32_e32 v84, 0, v203
	v_pk_add_f32 v[208:209], v[98:99], v[98:99] op_sel:[0,1] op_sel_hi:[1,0]
	s_waitcnt lgkmcnt(1)
	v_cndmask_b32_e64 v98, 0, v87, s[0:1]
	v_add_f32_e32 v98, v113, v98
	ds_bpermute_b32 v111, v220, v208
	v_sub_f32_e32 v97, v98, v97
	v_sub_f32_e32 v95, v97, v95
	v_sub_f32_e32 v96, v95, v96
	v_sub_f32_e32 v94, v96, v94
	v_fmac_f32_e32 v96, 0x3e0293ee, v81
	s_waitcnt lgkmcnt(1)
	v_add_f32_e32 v81, v85, v221
	v_mov_b32_e32 v85, v210
	v_xor_b32_e32 v112, 0x80000000, v219
	v_fmac_f32_e32 v97, 0x3e0293ee, v83
	v_fmac_f32_e32 v95, 0x3e0293ee, v82
	v_pk_add_f32 v[82:83], v[84:85], v[86:87]
	s_waitcnt lgkmcnt(0)
	v_cndmask_b32_e64 v211, 0, v111, s[0:1]
	v_pk_add_f32 v[86:87], v[112:113], v[82:83]
	v_pk_add_f32 v[84:85], v[112:113], v[82:83] neg_lo:[0,1] neg_hi:[0,1]
	v_add_f32_e32 v83, v211, v87
	v_sub_f32_e32 v83, v83, v207
	v_fmac_f32_e32 v94, 0x3e0293ee, v80
	v_pk_add_f32 v[208:209], v[208:209], v[110:111] op_sel_hi:[0,1]
	v_sub_f32_e32 v86, v83, v93
	v_exp_f32_e32 v99, v97
	v_exp_f32_e32 v98, v95
	v_exp_f32_e32 v97, v96
	v_exp_f32_e32 v96, v94
	v_mov_b32_e32 v85, v87
	v_sub_f32_e64 v94, -v218, v68
	v_mov_b32_e32 v95, v209
	v_sub_f32_e32 v87, v86, v206
	v_cndmask_b32_e64 v212, 0, v221, s[0:1]
	v_pk_add_f32 v[84:85], v[94:95], v[84:85]
	v_sub_f32_e32 v92, v87, v92
	ds_bpermute_b32 v80, v220, v84
	v_fmac_f32_e32 v92, 0x3e0293ee, v76
	v_add_f32_e32 v76, v212, v85
	v_sub_f32_e32 v76, v76, v91
	v_fmac_f32_e32 v87, 0x3e0293ee, v77
	v_sub_f32_e32 v77, v76, v89
	v_fmac_f32_e32 v86, 0x3e0293ee, v78
	v_sub_f32_e32 v78, v77, v90
	v_fmac_f32_e32 v83, 0x3e0293ee, v79
	v_sub_f32_e32 v79, v78, v88
	v_fmac_f32_e32 v77, 0x3e0293ee, v74
	v_fmac_f32_e32 v78, 0x3e0293ee, v73
	v_fmac_f32_e32 v79, 0x3e0293ee, v72
	s_waitcnt lgkmcnt(0)
	v_cndmask_b32_e64 v74, 0, v80, s[0:1]
	v_pk_add_f32 v[72:73], v[84:85], v[80:81]
	v_fmac_f32_e32 v76, 0x3e0293ee, v75
	v_add_f32_e32 v74, v74, v73
	v_sub_f32_e32 v74, v74, v219
	v_sub_f32_e32 v75, v74, v82
	v_exp_f32_e32 v91, v76
	v_sub_f32_e32 v76, v75, v218
	v_exp_f32_e32 v90, v77
	v_sub_f32_e32 v77, v76, v68
	v_fmac_f32_e32 v74, 0x3e0293ee, v71
	v_fmac_f32_e32 v75, 0x3e0293ee, v70
	v_fmac_f32_e32 v76, 0x3e0293ee, v69
	v_add_f32_e32 v69, v205, v77
	v_exp_f32_e32 v95, v83
	v_exp_f32_e32 v94, v86
	v_exp_f32_e32 v93, v87
	v_exp_f32_e32 v92, v92
	v_exp_f32_e32 v89, v78
	v_exp_f32_e32 v88, v79
	v_exp_f32_e32 v87, v74
	v_exp_f32_e32 v86, v75
	v_exp_f32_e32 v85, v76
	v_exp_f32_e32 v84, v69
	v_add_f32_e32 v111, v72, v73
	s_mov_b64 s[6:7], 0

; #define SBAR() __builtin_amdgcn_sched_barrier(0)
; #define ATT_RDK(X, KS) do { X##0 = tr_read<v_rd_off(0, KS, 0)>(vb); X##1 = tr_read<v_rd_off(0, KS, 1)>(vb); X##2 = tr_read<v_rd_off(1, KS, 0)>(vb); X##3 = tr_read<v_rd_off(1, KS, 1)>(vb); \
;     X##4 = tr_read<v_rd_off(2, KS, 0)>(vb); X##5 = tr_read<v_rd_off(2, KS, 1)>(vb); X##6 = tr_read<v_rd_off(3, KS, 0)>(vb); X##7 = tr_read<v_rd_off(3, KS, 1)>(vb); } while (0)
; #define ATT_MMAK(PA, X) do { o[0] = __builtin_amdgcn_mfma_f32_32x32x16_bf16(PA, ATT_PKV(X##0, X##1), o[0], 0, 0, 0); o[1] = __builtin_amdgcn_mfma_f32_32x32x16_bf16(PA, ATT_PKV(X##2, X##3), o[1], 0, 0, 0); \
;     o[2] = __builtin_amdgcn_mfma_f32_32x32x16_bf16(PA, ATT_PKV(X##4, X##5), o[2], 0, 0, 0); o[3] = __builtin_amdgcn_mfma_f32_32x32x16_bf16(PA, ATT_PKV(X##6, X##7), o[3], 0, 0, 0); } while (0)
; template <int BLK> __device__ __forceinline__ void pv_half(f32x16* o, int vb, bf16x8 paA, bf16x8 paB) {
;     s16x4 a0, a1, a2, a3, a4, a5, a6, a7, b0, b1, b2, b3, b4, b5, b6, b7;
;     SBAR(); ATT_RDK(a, 2 * BLK); ATT_RDK(b, 2 * BLK + 1);
;     asm volatile("s_waitcnt lgkmcnt(8)" ::: "memory"); SBAR(); ATT_MMAK(paA, a);
;     asm volatile("s_waitcnt lgkmcnt(0)" ::: "memory"); SBAR(); ATT_MMAK(paB, b);
; }
; __device__ __forceinline__ void sb_unit(LAS unsigned char* lds, const bf16* __restrict__ Q, const bf16* __restrict__ Kp, const bf16* __restrict__ Vp, const float* __restrict__ gsb,
;                                         bf16* __restrict__ mixed, int b, int h, int qt, int tid, int wave, int lane) {
;     ...
;                 bf16x8 paA, paB; ATT_PK4(p, 0, paA); ATT_PK4(p, 8, paB);
;                 pv_half<0>(o, vb0 + buf * SHM_T, paA, paB); }
;             carry = running;
;             done = __all(carry < SB_THR2);
.LBB0_623:
	v_cvt_pk_bf16_f32 v68, v84, v85
	v_cvt_pk_bf16_f32 v69, v86, v87
	v_cvt_pk_bf16_f32 v70, v88, v89
	v_cvt_pk_bf16_f32 v71, v90, v91
	v_cvt_pk_bf16_f32 v72, v92, v93
	v_cvt_pk_bf16_f32 v73, v94, v95
	v_cvt_pk_bf16_f32 v74, v96, v97
	v_cvt_pk_bf16_f32 v75, v98, v99
	v_permlane32_swap_b32_e32 v68, v70
	v_permlane32_swap_b32_e32 v69, v71
	v_permlane32_swap_b32_e32 v72, v74
	v_permlane32_swap_b32_e32 v73, v75
	ds_read_b64_tr_b16 v[76:77], v3 offset:0
	ds_read_b64_tr_b16 v[78:79], v3 offset:0x800
	ds_read_b64_tr_b16 v[80:81], v3 offset:0x200
	ds_read_b64_tr_b16 v[82:83], v3 offset:0xa00
	ds_read_b64_tr_b16 v[84:85], v3 offset:0x400
	ds_read_b64_tr_b16 v[86:87], v3 offset:0xc00
	ds_read_b64_tr_b16 v[88:89], v3 offset:0x600
	ds_read_b64_tr_b16 v[90:91], v3 offset:0xe00
	ds_read_b64_tr_b16 v[92:93], v3 offset:0x1000
	ds_read_b64_tr_b16 v[94:95], v3 offset:0x1800
	ds_read_b64_tr_b16 v[96:97], v3 offset:0x1200
	ds_read_b64_tr_b16 v[98:99], v3 offset:0x1a00
	ds_read_b64_tr_b16 v[190:191], v3 offset:0x1400
	ds_read_b64_tr_b16 v[192:193], v3 offset:0x1c00
	ds_read_b64_tr_b16 v[196:197], v3 offset:0x1600
	ds_read_b64_tr_b16 v[198:199], v3 offset:0x1e00
	s_waitcnt lgkmcnt(8)
	s_nop 0
	s_setprio 1
	v_mfma_f32_32x32x16_bf16 v[52:67], v[68:71], v[76:79], v[52:67]
	s_waitcnt lgkmcnt(0)
	v_mfma_f32_32x32x16_bf16 v[20:35], v[68:71], v[80:83], v[20:35]
	v_mfma_f32_32x32x16_bf16 v[36:51], v[68:71], v[84:87], v[36:51]
	v_mfma_f32_32x32x16_bf16 v[4:19], v[68:71], v[88:91], v[4:19]
	v_mfma_f32_32x32x16_bf16 v[52:67], v[72:75], v[92:95], v[52:67]
	v_cmp_gt_f32_e32 vcc, s61, v111
	s_cmp_eq_u64 vcc, exec
	s_cselect_b64 s[6:7], -1, 0
	v_mfma_f32_32x32x16_bf16 v[20:35], v[72:75], v[96:99], v[20:35]
	v_mfma_f32_32x32x16_bf16 v[36:51], v[72:75], v[190:193], v[36:51]
	v_mfma_f32_32x32x16_bf16 v[4:19], v[72:75], v[196:199], v[4:19]
	s_setprio 0
